# speedup vs baseline: 1.0066x; 1.0025x over previous
.LBB1_9:
	v_add_u32_e32 v182, s20, v209
	ds_read_b64_tr_b16 v[178:179], v182 offset:24576
	ds_read_b64_tr_b16 v[180:181], v182 offset:25088
	s_waitcnt lgkmcnt(9)
	v_mfma_f32_32x32x16_f16 v[98:113], v[174:177], v[142:145], v[34:49]
	v_add_f32_e32 v82, v66, v67
	v_add_f32_e32 v82, v68, v82
	v_add_f32_e32 v82, v69, v82
	v_add_f32_e32 v82, v70, v82
	v_add_f32_e32 v82, v71, v82
	v_cvt_pk_f16_f32 v134, v66, v67
	v_cvt_pk_f16_f32 v135, v68, v69
	ds_read_b64_tr_b16 v[174:175], v182 offset:28672
	ds_read_b64_tr_b16 v[176:177], v182 offset:29184
	v_add_f32_e32 v66, v72, v82
	s_waitcnt lgkmcnt(10)
	v_mfma_f32_32x32x16_f16 v[82:97], v[170:173], v[142:145], v[34:49]
	v_add_f32_e32 v66, v73, v66
	v_add_f32_e32 v66, v74, v66
	v_add_f32_e32 v66, v75, v66
	v_cvt_pk_f16_f32 v136, v70, v71
	v_cvt_pk_f16_f32 v137, v72, v73
	ds_read_b64_tr_b16 v[170:171], v182 offset:25600
	ds_read_b64_tr_b16 v[172:173], v182 offset:26112
	s_waitcnt lgkmcnt(11)
	v_mfma_f32_32x32x16_f16 v[98:113], v[166:169], v[138:141], v[98:113]
	v_add_f32_e32 v66, v76, v66
	v_add_f32_e32 v66, v77, v66
	v_add_f32_e32 v66, v78, v66
	v_add_f32_e32 v66, v79, v66
	v_cvt_pk_f16_f32 v126, v74, v75
	v_cvt_pk_f16_f32 v127, v76, v77
	ds_read_b64_tr_b16 v[74:75], v182 offset:29696
	ds_read_b64_tr_b16 v[76:77], v182 offset:30208
	s_waitcnt lgkmcnt(12)
	v_mfma_f32_32x32x16_f16 v[82:97], v[162:165], v[138:141], v[82:97]
	v_add_f32_e32 v66, v80, v66
	v_add_f32_e32 v66, v81, v66
	v_add_f32_e32 v66, v50, v66
	v_add_f32_e32 v66, v51, v66
	v_cvt_pk_f16_f32 v128, v78, v79
	v_cvt_pk_f16_f32 v129, v80, v81
	ds_read_b64_tr_b16 v[70:71], v182 offset:26624
	ds_read_b64_tr_b16 v[72:73], v182 offset:27136
	s_waitcnt lgkmcnt(13)
	v_mfma_f32_32x32x16_f16 v[98:113], v[158:161], v[130:133], v[98:113]
	v_add_f32_e32 v66, v52, v66
	v_add_f32_e32 v66, v53, v66
	v_add_f32_e32 v66, v54, v66
	v_add_f32_e32 v78, v55, v66
	v_cvt_pk_f16_f32 v118, v50, v51
	v_cvt_pk_f16_f32 v119, v52, v53
	ds_read_b64_tr_b16 v[66:67], v182 offset:30720
	ds_read_b64_tr_b16 v[68:69], v182 offset:31232
	s_waitcnt lgkmcnt(14)
	v_mfma_f32_32x32x16_f16 v[82:97], v[154:157], v[130:133], v[82:97]
	v_add_f32_e32 v50, v56, v78
	v_add_f32_e32 v50, v57, v50
	v_add_f32_e32 v50, v58, v50
	v_add_f32_e32 v50, v59, v50
	v_cvt_pk_f16_f32 v120, v54, v55
	v_cvt_pk_f16_f32 v121, v56, v57
	ds_read_b64_tr_b16 v[54:55], v182 offset:27648
	ds_read_b64_tr_b16 v[56:57], v182 offset:28160
	s_waitcnt lgkmcnt(14)
	v_mfma_f32_32x32x16_f16 v[98:113], v[150:153], v[122:125], v[98:113]
	v_add_f32_e32 v50, v60, v50
	v_add_f32_e32 v50, v61, v50
	v_add_f32_e32 v50, v62, v50
	v_add_f32_e32 v78, v63, v50
	v_cvt_pk_f16_f32 v114, v58, v59
	v_cvt_pk_f16_f32 v115, v60, v61
	ds_read_b64_tr_b16 v[50:51], v182 offset:31744
	ds_read_b64_tr_b16 v[52:53], v182 offset:32256
	v_mfma_f32_32x32x16_f16 v[82:97], v[146:149], v[122:125], v[82:97]
	v_add_f32_e32 v58, v64, v78
	v_add_f32_e32 v58, v65, v58
	v_add_f32_e32 v58, 0, v58
	v_cvt_pk_f16_f32 v116, v62, v63
	v_cvt_pk_f16_f32 v117, v64, v65
	v_max_f32_e32 v59, v98, v99
	v_max3_f32 v60, v100, v101, v102
	v_max3_f32 v59, v59, v103, v104
	v_max3_f32 v60, v60, v105, v106
	v_max3_f32 v59, v59, v107, v108
	v_max3_f32 v60, v60, v109, v110
	v_max3_f32 v59, v59, v111, v112
	v_add_f32_e32 v182, v203, v58
	v_max3_f32 v60, v60, v113, v82
	v_max3_f32 v59, v59, v83, v84
	v_max3_f32 v60, v60, v85, v86
	v_max3_f32 v59, v59, v87, v88
	v_max3_f32 v60, v60, v89, v90
	v_max3_f32 v59, v59, v91, v92
	v_max3_f32 v60, v60, v93, v94
	v_max3_f32 v59, v59, v95, v96
	v_max3_f32 v58, v59, v60, v97
	v_mov_b32_e32 v59, v58
	s_nop 1
	v_permlane32_swap_b32_e32 v58, v59
	s_add_u32 s2, s16, 0xffffe000
	s_addc_u32 s3, s17, -1
	s_add_i32 s20, s24, s39
	s_mov_b32 s21, m0
	s_mov_b32 m0, s20
	s_nop 0
	global_load_lds_dwordx4 v211, s[2:3]
	s_mov_b32 m0, s21
	v_max_f32_e32 v58, v58, v59
	s_add_i32 s2, s22, s40
	s_mov_b32 s3, m0
	s_mov_b32 m0, s2
	s_nop 0
	global_load_lds_dwordx4 v211, s[18:19]
	s_mov_b32 m0, s3
	v_cmp_lt_f32_e32 vcc, s23, v58
	s_cmp_lg_u64 vcc, 0
	s_cselect_b64 s[2:3], -1, 0
	s_cbranch_vccnz .LBB1_17

.LBB1_12:
	s_add_i32 s2, s22, 0x2000
	s_cmpk_lg_i32 s22, 0x4000
	s_cselect_b32 s43, s2, 0
	v_add_u32_e32 v183, s24, v209
	ds_read_b64_tr_b16 v[154:155], v183 offset:24576
	ds_read_b64_tr_b16 v[156:157], v183 offset:25088
	s_waitcnt lgkmcnt(9)
	v_mfma_f32_32x32x16_f16 v[66:81], v[58:61], v[142:145], v[34:49]
	v_add_f32_e32 v50, v98, v99
	v_add_f32_e32 v50, v100, v50
	v_add_f32_e32 v50, v101, v50
	v_add_f32_e32 v50, v102, v50
	v_add_f32_e32 v50, v103, v50
	v_cvt_pk_f16_f32 v134, v98, v99
	v_cvt_pk_f16_f32 v135, v100, v101
	ds_read_b64_tr_b16 v[150:151], v183 offset:28672
	ds_read_b64_tr_b16 v[152:153], v183 offset:29184
	v_add_f32_e32 v50, v104, v50
	v_add_f32_e32 v50, v105, v50
	v_add_f32_e32 v50, v106, v50
	v_add_f32_e32 v98, v107, v50
	s_waitcnt lgkmcnt(10)
	v_mfma_f32_32x32x16_f16 v[50:65], v[146:149], v[142:145], v[34:49]
	v_cvt_pk_f16_f32 v136, v102, v103
	v_cvt_pk_f16_f32 v137, v104, v105
	ds_read_b64_tr_b16 v[146:147], v183 offset:25600
	ds_read_b64_tr_b16 v[148:149], v183 offset:26112
	s_waitcnt lgkmcnt(11)
	v_mfma_f32_32x32x16_f16 v[66:81], v[178:181], v[138:141], v[66:81]
	v_add_f32_e32 v98, v108, v98
	v_add_f32_e32 v98, v109, v98
	v_add_f32_e32 v98, v110, v98
	v_add_f32_e32 v98, v111, v98
	v_cvt_pk_f16_f32 v126, v106, v107
	v_cvt_pk_f16_f32 v127, v108, v109
	ds_read_b64_tr_b16 v[106:107], v183 offset:29696
	ds_read_b64_tr_b16 v[108:109], v183 offset:30208
	s_waitcnt lgkmcnt(12)
	v_mfma_f32_32x32x16_f16 v[50:65], v[170:173], v[138:141], v[50:65]
	v_add_f32_e32 v98, v112, v98
	v_add_f32_e32 v98, v113, v98
	v_add_f32_e32 v98, v82, v98
	v_add_f32_e32 v98, v83, v98
	v_cvt_pk_f16_f32 v128, v110, v111
	v_cvt_pk_f16_f32 v129, v112, v113
	ds_read_b64_tr_b16 v[102:103], v183 offset:26624
	ds_read_b64_tr_b16 v[104:105], v183 offset:27136
	s_waitcnt lgkmcnt(13)
	v_mfma_f32_32x32x16_f16 v[66:81], v[174:177], v[130:133], v[66:81]
	v_add_f32_e32 v98, v84, v98
	v_add_f32_e32 v98, v85, v98
	v_add_f32_e32 v98, v86, v98
	v_add_f32_e32 v110, v87, v98
	v_cvt_pk_f16_f32 v118, v82, v83
	v_cvt_pk_f16_f32 v119, v84, v85
	ds_read_b64_tr_b16 v[98:99], v183 offset:30720
	ds_read_b64_tr_b16 v[100:101], v183 offset:31232
	s_waitcnt lgkmcnt(14)
	v_mfma_f32_32x32x16_f16 v[50:65], v[162:165], v[130:133], v[50:65]
	v_add_f32_e32 v82, v88, v110
	v_add_f32_e32 v82, v89, v82
	v_add_f32_e32 v82, v90, v82
	v_add_f32_e32 v82, v91, v82
	v_cvt_pk_f16_f32 v120, v86, v87
	v_cvt_pk_f16_f32 v121, v88, v89
	ds_read_b64_tr_b16 v[86:87], v183 offset:27648
	ds_read_b64_tr_b16 v[88:89], v183 offset:28160
	s_waitcnt lgkmcnt(14)
	v_mfma_f32_32x32x16_f16 v[66:81], v[166:169], v[122:125], v[66:81]
	v_add_f32_e32 v82, v92, v82
	v_add_f32_e32 v82, v93, v82
	v_add_f32_e32 v82, v94, v82
	v_add_f32_e32 v110, v95, v82
	v_cvt_pk_f16_f32 v114, v90, v91
	v_cvt_pk_f16_f32 v115, v92, v93
	ds_read_b64_tr_b16 v[82:83], v183 offset:31744
	ds_read_b64_tr_b16 v[84:85], v183 offset:32256
	v_mfma_f32_32x32x16_f16 v[50:65], v[158:161], v[122:125], v[50:65]
	v_add_f32_e32 v90, v96, v110
	v_add_f32_e32 v90, v97, v90
	v_add_f32_e32 v90, 0, v90
	v_cvt_pk_f16_f32 v116, v94, v95
	v_cvt_pk_f16_f32 v117, v96, v97
	v_max_f32_e32 v91, v66, v67
	v_max3_f32 v92, v68, v69, v70
	v_max3_f32 v91, v91, v71, v72
	v_max3_f32 v92, v92, v73, v74
	v_max3_f32 v91, v91, v75, v76
	v_max3_f32 v92, v92, v77, v78
	v_max3_f32 v91, v91, v79, v80
	v_add_f32_e32 v203, v182, v90
	v_max3_f32 v92, v92, v81, v50
	v_max3_f32 v91, v91, v51, v52
	v_max3_f32 v92, v92, v53, v54
	v_max3_f32 v91, v91, v55, v56
	v_max3_f32 v92, v92, v57, v58
	v_max3_f32 v91, v91, v59, v60
	v_max3_f32 v92, v92, v61, v62
	v_max3_f32 v91, v91, v63, v64
	v_max3_f32 v90, v91, v92, v65
	v_mov_b32_e32 v91, v90
	s_nop 1
	v_permlane32_swap_b32_e32 v90, v91
	s_add_i32 s2, s22, s39
	s_mov_b32 s3, m0
	s_mov_b32 m0, s2
	s_nop 0
	global_load_lds_dwordx4 v211, s[16:17]
	s_mov_b32 m0, s3
	s_add_u32 s2, s18, 0x2000
	v_max_f32_e32 v90, v90, v91
	s_addc_u32 s3, s19, 0
	s_add_i32 s20, s43, s40
	s_mov_b32 s21, m0
	s_mov_b32 m0, s20
	s_nop 0
	global_load_lds_dwordx4 v211, s[2:3]
	s_mov_b32 m0, s21
	v_cmp_lt_f32_e32 vcc, s23, v90
	s_cmp_lg_u64 vcc, 0
	s_cselect_b64 s[2:3], -1, 0
	s_cbranch_vccnz .LBB1_20

.LBB1_87:
	v_add_u32_e32 v65, s6, v251
	ds_read_b64_tr_b16 v[192:193], v65
	ds_read_b64_tr_b16 v[194:195], v65 offset:512
	s_waitcnt lgkmcnt(9)
	v_mfma_f32_32x32x16_f16 v[112:127], v[188:191], v[140:143], v[32:47]
	v_add_f32_e32 v66, v80, v81
	v_add_f32_e32 v66, v82, v66
	v_add_f32_e32 v66, v83, v66
	v_add_f32_e32 v66, v84, v66
	v_add_f32_e32 v66, v85, v66
	v_cvt_pk_f16_f32 v156, v80, v81
	v_cvt_pk_f16_f32 v157, v82, v83
	ds_read_b64_tr_b16 v[188:189], v65 offset:4096
	ds_read_b64_tr_b16 v[190:191], v65 offset:4608
	s_waitcnt lgkmcnt(10)
	v_mfma_f32_32x32x16_f16 v[96:111], v[184:187], v[140:143], v[32:47]
	v_add_f32_e32 v66, v86, v66
	v_add_f32_e32 v66, v87, v66
	v_add_f32_e32 v66, v88, v66
	v_add_f32_e32 v66, v89, v66
	v_cvt_pk_f16_f32 v158, v84, v85
	v_cvt_pk_f16_f32 v159, v86, v87
	ds_read_b64_tr_b16 v[78:79], v65 offset:1024
	ds_read_b64_tr_b16 v[80:81], v65 offset:1536
	s_waitcnt lgkmcnt(11)
	v_mfma_f32_32x32x16_f16 v[112:127], v[180:183], v[136:139], v[112:127]
	v_add_f32_e32 v66, v90, v66
	v_add_f32_e32 v66, v91, v66
	v_add_f32_e32 v66, v92, v66
	v_add_f32_e32 v66, v93, v66
	v_cvt_pk_f16_f32 v152, v88, v89
	v_cvt_pk_f16_f32 v153, v90, v91
	ds_read_b64_tr_b16 v[74:75], v65 offset:5120
	ds_read_b64_tr_b16 v[76:77], v65 offset:5632
	s_waitcnt lgkmcnt(12)
	v_mfma_f32_32x32x16_f16 v[96:111], v[176:179], v[136:139], v[96:111]
	v_add_f32_e32 v66, v94, v66
	v_add_f32_e32 v66, v95, v66
	v_add_f32_e32 v66, v48, v66
	v_add_f32_e32 v66, v49, v66
	v_cvt_pk_f16_f32 v154, v92, v93
	v_cvt_pk_f16_f32 v155, v94, v95
	ds_read_b64_tr_b16 v[70:71], v65 offset:2048
	ds_read_b64_tr_b16 v[72:73], v65 offset:2560
	s_waitcnt lgkmcnt(13)
	v_mfma_f32_32x32x16_f16 v[112:127], v[172:175], v[132:135], v[112:127]
	v_add_f32_e32 v66, v50, v66
	v_add_f32_e32 v66, v51, v66
	v_add_f32_e32 v66, v52, v66
	v_add_f32_e32 v82, v53, v66
	v_cvt_pk_f16_f32 v148, v48, v49
	v_cvt_pk_f16_f32 v149, v50, v51
	ds_read_b64_tr_b16 v[66:67], v65 offset:6144
	ds_read_b64_tr_b16 v[68:69], v65 offset:6656
	s_waitcnt lgkmcnt(14)
	v_mfma_f32_32x32x16_f16 v[96:111], v[168:171], v[132:135], v[96:111]
	v_add_f32_e32 v48, v54, v82
	v_add_f32_e32 v48, v55, v48
	v_add_f32_e32 v48, v56, v48
	v_add_f32_e32 v48, v57, v48
	v_cvt_pk_f16_f32 v150, v52, v53
	v_cvt_pk_f16_f32 v151, v54, v55
	ds_read_b64_tr_b16 v[52:53], v65 offset:3072
	ds_read_b64_tr_b16 v[54:55], v65 offset:3584
	s_waitcnt lgkmcnt(14)
	v_mfma_f32_32x32x16_f16 v[112:127], v[164:167], v[128:131], v[112:127]
	v_add_f32_e32 v48, v58, v48
	v_add_f32_e32 v48, v59, v48
	v_add_f32_e32 v48, v60, v48
	v_add_f32_e32 v82, v61, v48
	v_cvt_pk_f16_f32 v144, v56, v57
	v_cvt_pk_f16_f32 v145, v58, v59
	ds_read_b64_tr_b16 v[48:49], v65 offset:7168
	ds_read_b64_tr_b16 v[50:51], v65 offset:7680
	v_mfma_f32_32x32x16_f16 v[96:111], v[160:163], v[128:131], v[96:111]
	v_add_f32_e32 v56, v62, v82
	v_add_f32_e32 v56, v63, v56
	v_add_f32_e32 v56, 0, v56
	v_cvt_pk_f16_f32 v146, v60, v61
	v_cvt_pk_f16_f32 v147, v62, v63
	v_max_f32_e32 v57, v112, v113
	v_max3_f32 v58, v114, v115, v116
	v_max3_f32 v57, v57, v117, v118
	v_max3_f32 v58, v58, v119, v120
	v_max3_f32 v57, v57, v121, v122
	v_max3_f32 v58, v58, v123, v124
	v_max3_f32 v57, v57, v125, v126
	v_add_f32_e32 v64, v64, v56
	v_max3_f32 v58, v58, v127, v96
	v_max3_f32 v57, v57, v97, v98
	v_max3_f32 v58, v58, v99, v100
	v_max3_f32 v57, v57, v101, v102
	v_max3_f32 v58, v58, v103, v104
	v_max3_f32 v57, v57, v105, v106
	v_max3_f32 v58, v58, v107, v108
	v_max3_f32 v57, v57, v109, v110
	v_max3_f32 v56, v57, v58, v111
	v_mov_b32_e32 v57, v56
	s_add_u32 s6, s4, 0xffffe000
	s_nop 0
	v_permlane32_swap_b32_e32 v56, v57
	s_addc_u32 s7, s5, -1
	s_add_i32 s8, s30, s22
	s_mov_b32 s9, m0
	s_mov_b32 m0, s8
	s_nop 0
	global_load_lds_dwordx4 v211, s[6:7]
	s_mov_b32 m0, s9
	s_add_u32 s6, s2, 0xffffe000
	v_max_f32_e32 v56, v56, v57
	s_addc_u32 s7, s3, -1
	s_add_i32 s8, s12, s23
	s_mov_b32 s9, m0
	s_mov_b32 m0, s8
	s_nop 0
	global_load_lds_dwordx4 v211, s[6:7]
	s_mov_b32 m0, s9
	v_cmp_lt_f32_e32 vcc, s17, v56
	s_cmp_lg_u64 vcc, 0
	s_cselect_b64 s[6:7], -1, 0
	s_cbranch_vccnz .LBB1_95

.LBB1_90:
	s_add_i32 s6, s12, 0x2000
	s_cmpk_lg_i32 s12, 0x4000
	s_cselect_b32 s25, s6, 0
	v_add_u32_e32 v65, s30, v251
	ds_read_b64_tr_b16 v[168:169], v65
	ds_read_b64_tr_b16 v[170:171], v65 offset:512
	s_waitcnt lgkmcnt(9)
	v_mfma_f32_32x32x16_f16 v[80:95], v[56:59], v[140:143], v[32:47]
	v_add_f32_e32 v48, v112, v113
	v_add_f32_e32 v48, v114, v48
	v_add_f32_e32 v48, v115, v48
	v_add_f32_e32 v48, v116, v48
	v_add_f32_e32 v48, v117, v48
	v_cvt_pk_f16_f32 v156, v112, v113
	v_cvt_pk_f16_f32 v157, v114, v115
	ds_read_b64_tr_b16 v[164:165], v65 offset:4096
	ds_read_b64_tr_b16 v[166:167], v65 offset:4608
	v_add_f32_e32 v48, v118, v48
	v_add_f32_e32 v48, v119, v48
	v_add_f32_e32 v48, v120, v48
	v_add_f32_e32 v66, v121, v48
	s_waitcnt lgkmcnt(10)
	v_mfma_f32_32x32x16_f16 v[48:63], v[160:163], v[140:143], v[32:47]
	v_cvt_pk_f16_f32 v158, v116, v117
	v_cvt_pk_f16_f32 v159, v118, v119
	ds_read_b64_tr_b16 v[160:161], v65 offset:1024
	ds_read_b64_tr_b16 v[162:163], v65 offset:1536
	s_waitcnt lgkmcnt(11)
	v_mfma_f32_32x32x16_f16 v[80:95], v[188:191], v[136:139], v[80:95]
	v_add_f32_e32 v66, v122, v66
	v_add_f32_e32 v66, v123, v66
	v_add_f32_e32 v66, v124, v66
	v_add_f32_e32 v66, v125, v66
	v_cvt_pk_f16_f32 v152, v120, v121
	v_cvt_pk_f16_f32 v153, v122, v123
	ds_read_b64_tr_b16 v[116:117], v65 offset:5120
	ds_read_b64_tr_b16 v[118:119], v65 offset:5632
	s_waitcnt lgkmcnt(12)
	v_mfma_f32_32x32x16_f16 v[48:63], v[184:187], v[136:139], v[48:63]
	v_add_f32_e32 v66, v126, v66
	v_add_f32_e32 v66, v127, v66
	v_add_f32_e32 v66, v96, v66
	v_add_f32_e32 v66, v97, v66
	v_cvt_pk_f16_f32 v154, v124, v125
	v_cvt_pk_f16_f32 v155, v126, v127
	ds_read_b64_tr_b16 v[112:113], v65 offset:2048
	ds_read_b64_tr_b16 v[114:115], v65 offset:2560
	s_waitcnt lgkmcnt(13)
	v_mfma_f32_32x32x16_f16 v[80:95], v[74:77], v[132:135], v[80:95]
	v_add_f32_e32 v66, v98, v66
	v_add_f32_e32 v66, v99, v66
	v_add_f32_e32 v66, v100, v66
	v_add_f32_e32 v66, v101, v66
	v_cvt_pk_f16_f32 v148, v96, v97
	v_cvt_pk_f16_f32 v149, v98, v99
	ds_read_b64_tr_b16 v[74:75], v65 offset:6144
	ds_read_b64_tr_b16 v[76:77], v65 offset:6656
	s_waitcnt lgkmcnt(14)
	v_mfma_f32_32x32x16_f16 v[48:63], v[176:179], v[132:135], v[48:63]
	v_add_f32_e32 v66, v102, v66
	v_add_f32_e32 v66, v103, v66
	v_add_f32_e32 v66, v104, v66
	v_add_f32_e32 v66, v105, v66
	v_cvt_pk_f16_f32 v150, v100, v101
	v_cvt_pk_f16_f32 v151, v102, v103
	ds_read_b64_tr_b16 v[70:71], v65 offset:3072
	ds_read_b64_tr_b16 v[72:73], v65 offset:3584
	s_waitcnt lgkmcnt(14)
	v_mfma_f32_32x32x16_f16 v[80:95], v[180:183], v[128:131], v[80:95]
	v_add_f32_e32 v66, v106, v66
	v_add_f32_e32 v66, v107, v66
	v_add_f32_e32 v66, v108, v66
	v_add_f32_e32 v78, v109, v66
	v_cvt_pk_f16_f32 v144, v104, v105
	v_cvt_pk_f16_f32 v145, v106, v107
	ds_read_b64_tr_b16 v[66:67], v65 offset:7168
	ds_read_b64_tr_b16 v[68:69], v65 offset:7680
	v_mfma_f32_32x32x16_f16 v[48:63], v[172:175], v[128:131], v[48:63]
	v_add_f32_e32 v65, v110, v78
	v_add_f32_e32 v65, v111, v65
	v_add_f32_e32 v65, 0, v65
	v_cvt_pk_f16_f32 v146, v108, v109
	v_cvt_pk_f16_f32 v147, v110, v111
	v_max_f32_e32 v78, v80, v81
	v_max3_f32 v79, v82, v83, v84
	v_max3_f32 v78, v78, v85, v86
	v_max3_f32 v79, v79, v87, v88
	v_max3_f32 v78, v78, v89, v90
	v_max3_f32 v79, v79, v91, v92
	v_max3_f32 v78, v78, v93, v94
	v_add_f32_e32 v64, v64, v65
	v_max3_f32 v79, v79, v95, v48
	v_max3_f32 v78, v78, v49, v50
	v_max3_f32 v79, v79, v51, v52
	v_max3_f32 v78, v78, v53, v54
	v_max3_f32 v79, v79, v55, v56
	v_max3_f32 v78, v78, v57, v58
	v_max3_f32 v79, v79, v59, v60
	v_max3_f32 v78, v78, v61, v62
	v_max3_f32 v65, v78, v79, v63
	v_mov_b32_e32 v78, v65
	s_nop 1
	v_permlane32_swap_b32_e32 v65, v78
	s_add_i32 s6, s12, s22
	s_mov_b32 s7, m0
	s_mov_b32 m0, s6
	s_nop 0
	global_load_lds_dwordx4 v211, s[4:5]
	s_mov_b32 m0, s7
	v_max_f32_e32 v65, v65, v78
	s_add_i32 s6, s25, s23
	s_mov_b32 s7, m0
	s_mov_b32 m0, s6
	s_nop 0
	global_load_lds_dwordx4 v211, s[2:3]
	s_mov_b32 m0, s7
	v_cmp_lt_f32_e32 vcc, s17, v65
	s_cmp_lg_u64 vcc, 0
	s_cselect_b64 s[6:7], -1, 0
	s_cbranch_vccnz .LBB1_98
